# adds phase 0 item mapping: the 8 waves of a workgroup take 8 adjacent column strips of the same 64 weight rows (assumes the 256-CU grid of this chip)
# baseline (speedup 1.0000x reference)
.LBB0_7:
	s_load_dwordx16 s[64:79], s[0:1], 0x50
	s_load_dwordx16 s[36:51], s[0:1], 0x90
	s_lshl_b32 s94, s97, 3
	s_cmp_lt_i32 s90, 1
	s_cselect_b64 s[0:1], -1, 0
	s_cmp_gt_i32 s91, 0
	s_waitcnt lgkmcnt(0)
	v_writelane_b32 v239, s36, 7
	s_cselect_b64 s[2:3], -1, 0
	s_lshl_b32 s83, s96, 3
	v_writelane_b32 v239, s37, 8
	v_writelane_b32 v239, s38, 9
	v_writelane_b32 v239, s39, 10
	v_writelane_b32 v239, s40, 11
	v_writelane_b32 v239, s41, 12
	v_writelane_b32 v239, s42, 13
	v_writelane_b32 v239, s43, 14
	v_writelane_b32 v239, s44, 15
	v_writelane_b32 v239, s45, 16
	v_writelane_b32 v239, s46, 17
	v_writelane_b32 v239, s47, 18
	v_writelane_b32 v239, s48, 19
	v_writelane_b32 v239, s49, 20
	v_writelane_b32 v239, s50, 21
	v_writelane_b32 v239, s51, 22
	v_writelane_b32 v239, s83, 23
	v_writelane_b32 v239, s88, 24
	s_and_b64 s[0:1], s[0:1], s[2:3]
	s_andn2_b64 vcc, exec, s[0:1]
	v_writelane_b32 v239, s89, 25
	v_writelane_b32 v239, s90, 26
	v_writelane_b32 v239, s91, 27
	s_cbranch_vccnz .LBB0_175
	v_mov_b32_e32 v1, v0
	s_lshl_b32 s39, s96, 9
	v_readfirstlane_b32 s0, v1
	s_ashr_i32 s0, s0, 6
	s_lshl_b32 s52, s97, 9
	s_and_b32 s62, s96, 31
	s_lshl_b32 s1, s0, 5
	s_or_b32 s62, s62, s1
	s_lshr_b32 s1, s96, 5
	s_lshl_b32 s1, s1, 8
	s_or_b32 s62, s62, s1
	s_mov_b32 s2, s94
	s_cmpk_lt_i32 s62, 0x7600
	v_writelane_b32 v239, s2, 28
	s_nop 1
	v_writelane_b32 v239, s3, 29
	s_cbranch_scc0 .LBB0_102
	s_mul_i32 s1, s0, 0x4100
	v_writelane_b32 v239, s33, 30
	s_add_i32 s41, s1, 0
	v_writelane_b32 v239, s1, 31
	s_add_u32 s1, s88, 0xd900000
	v_writelane_b32 v239, s1, 33
	s_addc_u32 s1, s89, 0
	v_writelane_b32 v239, s1, 35
	s_add_u32 s1, s88, 0xb900000
	v_writelane_b32 v239, s1, 37
	s_addc_u32 s1, s89, 0
	v_writelane_b32 v239, s1, 39
	s_add_u32 s1, s88, 0x7900000
	v_writelane_b32 v239, s1, 40
	s_addc_u32 s1, s89, 0
	s_add_u32 s95, s88, 0x100000
	v_writelane_b32 v239, s1, 42
	s_addc_u32 s44, s89, 0
	s_lshl_b32 s3, s62, 6
	s_lshl_b32 s9, s62, 1
	s_lshl_b32 s0, s62, 2
	v_and_b32_e32 v136, 63, v1
	s_mov_b32 s92, 0
	v_writelane_b32 v239, s96, 44
	s_lshl_b32 s96, s97, 4
	s_add_i32 s36, s0, 0xffff4400
	s_lshl_b32 s2, s97, 5
	s_mov_b64 s[0:1], 0
	s_mov_b32 s37, s3
	s_mov_b32 s33, s62
	s_mov_b64 s[4:5], 0
	s_mov_b32 s91, 0
	s_mov_b32 s6, 0
	s_mov_b32 s8, 0
	s_mov_b32 s60, 0
	s_mov_b32 s61, 0
	s_mov_b32 s40, s95
